# v69 + fox tile loop: O accumulators stay in the MFMA registers; per-tile 32 x v_mov copy removed, reference-move path scales in place
# speedup vs baseline: 1.0079x; 1.0079x over previous
.LBB0_299:
	s_andn2_b64 vcc, exec, s[8:9]
	s_cbranch_vccnz .LBB0_303
	v_add_f32_e32 v140, v242, v244
	v_bfe_u32 v141, v140, 16, 1
	v_add3_u32 v142, v140, v141, s71
	v_and_b32_e32 v141, 0xffff0000, v142
	v_sub_f32_e32 v140, v140, v141
	v_bfe_u32 v143, v140, 16, 1
	v_add3_u32 v143, v140, v143, s71
	v_and_b32_e32 v140, 0xffff0000, v143
	v_add_f32_e32 v243, v141, v140
	v_sub_f32_e32 v140, v243, v242
	v_exp_f32_e64 v141, -v140
	s_and_saveexec_b64 s[8:9], s[4:5]
	ds_write_b32 v189, v141
	s_or_b64 exec, exec, s[8:9]
	s_waitcnt lgkmcnt(0)
	ds_read_b128 v[144:147], v190 offset:64
	ds_read_b128 v[148:151], v190 offset:96
	ds_read_b128 v[244:247], v190
	ds_read_b128 v[248:251], v190 offset:32
	v_perm_b32 v142, v143, v142, s72
	v_xor_b32_e32 v142, 0x80008000, v142
	v_pk_add_f32 v[48:49], v[48:49], v[140:141] op_sel_hi:[1,0] neg_lo:[0,1] neg_hi:[0,1]
	v_pk_add_f32 v[32:33], v[32:33], v[140:141] op_sel_hi:[1,0] neg_lo:[0,1] neg_hi:[0,1]
	v_pk_add_f32 v[50:51], v[50:51], v[140:141] op_sel_hi:[1,0] neg_lo:[0,1] neg_hi:[0,1]
	v_pk_add_f32 v[34:35], v[34:35], v[140:141] op_sel_hi:[1,0] neg_lo:[0,1] neg_hi:[0,1]
	v_pk_add_f32 v[52:53], v[52:53], v[140:141] op_sel_hi:[1,0] neg_lo:[0,1] neg_hi:[0,1]
	v_pk_add_f32 v[36:37], v[36:37], v[140:141] op_sel_hi:[1,0] neg_lo:[0,1] neg_hi:[0,1]
	v_pk_add_f32 v[54:55], v[54:55], v[140:141] op_sel_hi:[1,0] neg_lo:[0,1] neg_hi:[0,1]
	v_pk_add_f32 v[38:39], v[38:39], v[140:141] op_sel_hi:[1,0] neg_lo:[0,1] neg_hi:[0,1]
	v_pk_add_f32 v[56:57], v[56:57], v[140:141] op_sel_hi:[1,0] neg_lo:[0,1] neg_hi:[0,1]
	v_pk_add_f32 v[40:41], v[40:41], v[140:141] op_sel_hi:[1,0] neg_lo:[0,1] neg_hi:[0,1]
	v_pk_add_f32 v[58:59], v[58:59], v[140:141] op_sel_hi:[1,0] neg_lo:[0,1] neg_hi:[0,1]
	v_pk_add_f32 v[42:43], v[42:43], v[140:141] op_sel_hi:[1,0] neg_lo:[0,1] neg_hi:[0,1]
	v_pk_add_f32 v[60:61], v[60:61], v[140:141] op_sel_hi:[1,0] neg_lo:[0,1] neg_hi:[0,1]
	v_pk_add_f32 v[44:45], v[44:45], v[140:141] op_sel_hi:[1,0] neg_lo:[0,1] neg_hi:[0,1]
	v_pk_add_f32 v[62:63], v[62:63], v[140:141] op_sel_hi:[1,0] neg_lo:[0,1] neg_hi:[0,1]
	v_pk_add_f32 v[46:47], v[46:47], v[140:141] op_sel_hi:[1,0] neg_lo:[0,1] neg_hi:[0,1]
	v_cndmask_b32_e64 v138, v142, v138, s[4:5]
	v_mul_f32_e32 v125, v125, v141
	s_waitcnt lgkmcnt(2)
	v_pk_mul_f32 v[14:15], v[14:15], v[150:151]
	v_pk_mul_f32 v[10:11], v[10:11], v[146:147]
	s_waitcnt lgkmcnt(0)
	v_pk_mul_f32 v[6:7], v[6:7], v[250:251]
	v_pk_mul_f32 v[2:3], v[2:3], v[246:247]
	v_pk_mul_f32 v[12:13], v[12:13], v[148:149]
	v_pk_mul_f32 v[8:9], v[8:9], v[144:145]
	v_pk_mul_f32 v[4:5], v[4:5], v[248:249]
	v_pk_mul_f32 v[0:1], v[0:1], v[244:245]
	v_pk_mul_f32 v[30:31], v[30:31], v[150:151]
	v_pk_mul_f32 v[26:27], v[26:27], v[146:147]
	v_pk_mul_f32 v[22:23], v[22:23], v[250:251]
	v_pk_mul_f32 v[18:19], v[18:19], v[246:247]
	v_pk_mul_f32 v[28:29], v[28:29], v[148:149]
	v_pk_mul_f32 v[24:25], v[24:25], v[144:145]
	v_pk_mul_f32 v[20:21], v[20:21], v[248:249]
	v_pk_mul_f32 v[16:17], v[16:17], v[244:245]
	s_branch .LBB0_304

.LBB0_304:
	v_exp_f32_e32 v140, v48
	v_exp_f32_e32 v141, v32
	v_exp_f32_e32 v142, v49
	v_exp_f32_e32 v143, v33
	v_exp_f32_e32 v144, v50
	v_exp_f32_e32 v145, v34
	v_exp_f32_e32 v146, v51
	v_exp_f32_e32 v147, v35
	v_add_f32_e32 v32, v141, v140
	v_exp_f32_e32 v148, v52
	v_exp_f32_e32 v149, v36
	v_add_f32_e32 v32, 0, v32
	v_add_f32_e32 v33, v143, v142
	v_exp_f32_e32 v34, v53
	v_exp_f32_e32 v48, v37
	v_add_f32_e32 v32, v33, v32
	v_add_f32_e32 v33, v145, v144
	v_add_f32_e32 v32, v33, v32
	v_add_f32_e32 v33, v147, v146
	v_add_f32_e32 v35, v33, v32
	v_add_f32_e32 v49, v149, v148
	v_pk_add_f32 v[32:33], v[48:49], v[34:35]
	v_exp_f32_e32 v35, v54
	v_pk_add_f32 v[36:37], v[32:33], v[32:33] op_sel_hi:[0,1]
	v_exp_f32_e32 v49, v38
	v_exp_f32_e32 v36, v55
	v_exp_f32_e32 v50, v39
	v_exp_f32_e32 v52, v41
	v_add_f32_e32 v51, v49, v35
	v_exp_f32_e32 v54, v43
	v_pk_add_f32 v[32:33], v[50:51], v[36:37]
	v_exp_f32_e32 v37, v56
	v_pk_add_f32 v[38:39], v[32:33], v[32:33] op_sel_hi:[0,1]
	v_exp_f32_e32 v51, v40
	v_exp_f32_e32 v38, v57
	v_exp_f32_e32 v56, v45
	v_cvt_pk_bf16_f32 v35, v35, v36
	v_add_f32_e32 v53, v51, v37
	v_pk_add_f32 v[32:33], v[52:53], v[38:39]
	v_exp_f32_e32 v39, v58
	v_pk_add_f32 v[40:41], v[32:33], v[32:33] op_sel_hi:[0,1]
	v_exp_f32_e32 v53, v42
	v_exp_f32_e32 v40, v59
	v_exp_f32_e32 v58, v47
	v_cvt_pk_bf16_f32 v36, v37, v38
	v_add_f32_e32 v55, v53, v39
	v_pk_add_f32 v[32:33], v[54:55], v[40:41]
	v_exp_f32_e32 v41, v60
	v_pk_add_f32 v[42:43], v[32:33], v[32:33] op_sel_hi:[0,1]
	v_exp_f32_e32 v55, v44
	v_exp_f32_e32 v42, v61
	v_cvt_pk_bf16_f32 v37, v39, v40
	v_add_u32_e32 v239, v239, v187
	v_add_f32_e32 v57, v55, v41
	v_pk_add_f32 v[32:33], v[56:57], v[42:43]
	v_exp_f32_e32 v43, v62
	v_pk_add_f32 v[44:45], v[32:33], v[32:33] op_sel_hi:[0,1]
	v_exp_f32_e32 v57, v46
	v_exp_f32_e32 v44, v63
	v_cvt_pk_bf16_f32 v38, v41, v42
	v_cvt_pk_bf16_f32 v42, v149, v48
	v_add_f32_e32 v59, v57, v43
	v_cvt_pk_bf16_f32 v39, v43, v44
	v_cvt_pk_bf16_f32 v43, v49, v50
	ds_read_b64_tr_b16 v[48:49],v241 offset:4096
	v_pk_add_f32 v[32:33], v[58:59], v[44:45]
	v_cvt_pk_bf16_f32 v44, v51, v52
	ds_read_b64_tr_b16 v[50:51],v241 offset:4608
	v_cvt_pk_bf16_f32 v45, v53, v54
	ds_read_b64_tr_b16 v[52:53],v241 offset:5120
	v_cvt_pk_bf16_f32 v46, v55, v56
	ds_read_b64_tr_b16 v[54:55],v241 offset:5632
	v_cvt_pk_bf16_f32 v47, v57, v58
	ds_read_b64_tr_b16 v[56:57],v241 offset:6144
	ds_read_b64_tr_b16 v[58:59],v241 offset:6656
	ds_read_b64_tr_b16 v[60:61],v241 offset:7168
	ds_read_b64_tr_b16 v[62:63],v241 offset:7680
	s_waitcnt lgkmcnt(8)
	v_add_f32_e32 v32, v32, v33
	v_add_f32_e32 v125, v125, v32
	v_cvt_pk_bf16_f32 v32, v140, v142
	v_cvt_pk_bf16_f32 v33, v144, v146
	v_cvt_pk_bf16_f32 v34, v148, v34
	v_cvt_pk_bf16_f32 v40, v141, v143
	v_cvt_pk_bf16_f32 v41, v145, v147
	v_mfma_f32_32x32x16_bf16 v[0:15], v[32:35], v[92:95], v[0:15]
	s_waitcnt lgkmcnt(0)
	v_mfma_f32_32x32x16_bf16 v[0:15], v[36:39], v[88:91], v[0:15]
	v_mfma_f32_32x32x16_bf16 v[0:15], v[40:43], v[84:87], v[0:15]
	v_mfma_f32_32x32x16_bf16 v[0:15], v[44:47], v[80:83], v[0:15]
	v_mfma_f32_32x32x16_bf16 v[16:31], v[32:35], v[48:51], v[16:31]
	s_add_i32 s8, s79, 1
	s_add_i32 s78, s78, 1
	s_and_b32 s79, s8, 3
	s_add_i32 s8, s51, s78
	s_cmp_ge_i32 s8, s75
	v_add_u32_e32 v240, 64, v240
	v_mfma_f32_32x32x16_bf16 v[16:31], v[36:39], v[52:55], v[16:31]
	v_mfma_f32_32x32x16_bf16 v[16:31], v[40:43], v[56:59], v[16:31]
	v_mfma_f32_32x32x16_bf16 v[16:31], v[44:47], v[60:63], v[16:31]
	s_cbranch_scc1 .LBB0_312
	s_nop 0
	v_mov_b32_e32 v242, v243
	s_andn2_b64 vcc, exec, s[28:29]
	s_add_i32 s42, s51, s78
	s_cbranch_vccz .LBB0_283
	s_branch .LBB0_287
